# P2 chunk-summary loop unrolled by two with the K/V tiles prefetched two units ahead (second register set)
# baseline (speedup 1.0000x reference)
; #define LAS __attribute__((address_space(3)))
; #define GAS __attribute__((address_space(1)))
; #define LAS __attribute__((address_space(3)))
; DI void ret_kv_phase(LAS unsigned char* lds, const bf16* PROJ, float* KVB, const float* ssqsb, float* rsb, int bx, int G, int tid) {
;     const int lane = tid & 63, w = __builtin_amdgcn_readfirstlane(tid >> 6), r = lane & 31, h = lane >> 5;
;     LAS unsigned char* KT = lds + L_KT; LAS unsigned char* VT = lds + L_VT;
;     const int te = w >> 1, td0 = 2 * (w & 1), which = (tid >> 7) & 1;
;     v4u kreg[4], vreg[4]; f32x4 pp = {0.f, 0.f, 0.f, 0.f};
;     if (bx < 2048) { const int n = bx & 63, hd = (bx >> 6) & 15, b = bx >> 10; const size_t m0 = (size_t)b * SEQ + 128 * n;
;         tile_ld(kreg, PROJ + m0 * INW + C_RK + 128 * hd, INW, tid); tile_ld(vreg, PROJ + m0 * INW + C_RV + 128 * hd, INW, tid);
;         pp = *(const GAS f32x4*)(ssqsb + ((m0 + (tid & 127)) * 32 + 16 * which + hd) * 4); }
.LBB0_396:
	s_cmp_lt_i32 s74, 3
	s_cselect_b64 s[0:1], -1, 0
	s_and_b64 s[4:5], s[0:1], s[4:5]
	s_andn2_b64 vcc, exec, s[4:5]
	s_cbranch_vccnz .LBB0_404
	s_cmpk_gt_i32 s2, 0x7ff
	v_readfirstlane_b32 s0, v0
	s_cbranch_scc1 .LBB0_404
	s_add_u32 s10, s84, 0xe00000
	s_addc_u32 s11, s85, 0
	s_add_u32 s12, s84, 0x600000
	s_addc_u32 s13, s85, 0
	s_ashr_i32 s6, s2, 10
	s_ashr_i32 s7, s6, 31
	s_lshl_b32 s22, s2, 7
	s_lshl_b64 s[6:7], s[6:7], 13
	s_and_b32 s8, s22, 0x1f80
	s_or_b32 s6, s6, s8
	s_mul_i32 s8, s7, 0x7000
	s_mul_hi_u32 s9, s6, 0x7000
	s_and_b32 s14, s0, 64
	s_lshr_b32 s1, s0, 7
	s_bfe_u32 s3, s2, 0x40006
	s_add_i32 s9, s9, s8
	s_mul_i32 s8, s6, 0x7000
	s_add_u32 s8, s42, s8
	s_addc_u32 s9, s43, s9
	s_lshl_b32 s16, s3, 8
	v_lshlrev_b32_e32 v2, 3, v0
	v_and_b32_e32 v2, 0x78, v2
	s_add_u32 s8, s8, s16
	v_or_b32_e32 v12, 0x200, v0
	v_mov_b32_e32 v71, 0
	v_lshlrev_b32_e32 v70, 1, v2
	s_addc_u32 s9, s9, 0
	v_lshrrev_b32_e32 v9, 4, v0
	v_lshrrev_b32_e32 v13, 4, v12
	v_lshl_add_u64 v[4:5], s[8:9], 0, v[70:71]
	s_mov_b64 s[16:17], 0x2000
	v_mul_u32_u24_e32 v8, 0x3800, v9
	v_mul_u32_u24_e32 v12, 0x3800, v13
	v_lshl_add_u64 v[6:7], v[4:5], 0, s[16:17]
	v_lshlrev_b32_e32 v70, 1, v8
	v_lshlrev_b32_e32 v14, 1, v12
	v_mov_b32_e32 v15, v71
	v_lshl_add_u64 v[10:11], v[6:7], 0, v[70:71]
	v_lshl_add_u64 v[16:17], v[6:7], 0, v[14:15]
	global_load_dwordx4 v[34:37], v[10:11], off
	global_load_dwordx4 v[38:41], v[16:17], off
	v_or_b32_e32 v16, 0x600, v0
	v_lshrrev_b32_e32 v17, 4, v16
	s_mov_b32 s23, 0x1c0000
	v_mul_u32_u24_e32 v16, 0x3800, v17
	v_add_co_u32_e32 v10, vcc, s23, v10
	v_lshlrev_b32_e32 v18, 1, v16
	v_mov_b32_e32 v19, v71
	s_mov_b64 s[18:19], 0x3000
	v_addc_co_u32_e32 v11, vcc, 0, v11, vcc
	v_lshl_add_u64 v[6:7], v[6:7], 0, v[18:19]
	v_lshl_add_u64 v[4:5], v[4:5], 0, s[18:19]
	global_load_dwordx4 v[42:45], v[10:11], off
	global_load_dwordx4 v[46:49], v[6:7], off
	v_lshl_add_u64 v[6:7], v[4:5], 0, v[70:71]
	v_lshl_add_u64 v[10:11], v[4:5], 0, v[14:15]
	global_load_dwordx4 v[50:53], v[6:7], off
	global_load_dwordx4 v[54:57], v[10:11], off
	v_add_co_u32_e32 v6, vcc, s23, v6
	v_lshl_add_u64 v[4:5], v[4:5], 0, v[18:19]
	s_nop 0
	v_addc_co_u32_e32 v7, vcc, 0, v7, vcc
	v_and_b32_e32 v72, 0x7f, v0
	global_load_dwordx4 v[58:61], v[6:7], off
	global_load_dwordx4 v[66:69], v[4:5], off
	v_or_b32_e32 v4, s6, v72
	v_mov_b32_e32 v5, s7
	v_lshrrev_b32_e32 v6, 3, v0
	v_lshlrev_b64 v[4:5], 5, v[4:5]
	v_and_b32_e32 v74, 16, v6
	v_or3_b32 v4, v4, s3, v74
	v_lshl_add_u64 v[4:5], v[4:5], 4, s[10:11]
	global_load_dwordx4 v[62:65], v[4:5], off
	v_lshlrev_b32_e32 v4, 4, v0
	v_lshlrev_b32_e32 v7, 2, v0
	v_and_b32_e32 v4, 0xf0, v4
	s_lshl_b32 s8, s1, 5
	v_and_b32_e32 v5, 4, v6
	v_and_b32_e32 v6, 16, v0
	v_and_b32_e32 v7, 12, v7
	v_add_u32_e32 v18, 0, v4
	v_lshrrev_b32_e32 v4, 2, v0
	v_or3_b32 v10, s8, v6, v7
	v_or3_b32 v6, v7, v6, s14
	s_movk_i32 s3, 0x140
	v_and_b32_e32 v76, 0x60, v4
	v_and_or_b32 v4, v4, 3, v5
	v_lshlrev_b32_e32 v73, 1, v6
	v_mov_b32_e32 v6, 0x6400
	v_mad_u32_u24 v22, v4, s3, v6
	v_mov_b32_e32 v6, 0x7800
	v_mad_u32_u24 v23, v4, s3, v6
	v_mov_b32_e32 v6, 0x8c00
	v_and_b32_e32 v3, 31, v0
	s_lshl_b32 s8, s1, 12
	v_mul_u32_u24_e32 v20, 0x140, v4
	v_mad_u32_u24 v75, v4, s3, 0
	v_mad_u32_u24 v24, v4, s3, v6
	v_lshlrev_b32_e32 v4, 6, v0
	v_and_b32_e32 v25, 0x800, v4
	v_or_b32_e32 v4, s8, v3
	v_lshlrev_b32_e32 v11, 7, v5
	s_lshl_b32 s0, s0, 2
	v_ashrrev_i32_e32 v5, 31, v4
	s_ashr_i32 s3, s2, 31
	s_and_b32 s0, s0, 0x100
	v_lshlrev_b64 v[6:7], 2, v[4:5]
	s_lshl_b64 s[20:21], s[2:3], 16
	v_or3_b32 v6, v25, s0, v6
	s_or_b32 s3, s8, s14
	v_lshl_add_u64 v[78:79], s[84:85], 0, v[6:7]
	v_or_b32_e32 v6, s3, v3
	v_or3_b32 v4, v11, s14, v4
	v_lshl_add_u32 v19, v10, 1, 0
	v_or_b32_e32 v10, v6, v11
	v_lshl_add_u64 v[4:5], v[4:5], 2, s[84:85]
	s_mov_b64 s[26:27], 0x42e00080
	v_lshl_add_u64 v[84:85], v[4:5], 0, s[26:27]
	v_or_b32_e32 v4, 0xc80, v10
	v_ashrrev_i32_e32 v5, 31, v4
	s_mov_b64 s[8:9], 0x42e00000
	v_lshl_add_u64 v[4:5], v[4:5], 2, s[84:85]
	v_ashrrev_i32_e32 v7, 31, v6
	v_lshl_add_u64 v[86:87], v[4:5], 0, s[8:9]
	v_lshlrev_b64 v[4:5], 2, v[6:7]
	v_or_b32_e32 v4, v4, v25
	v_lshl_add_u64 v[4:5], s[84:85], 0, v[4:5]
	s_mov_b64 s[26:27], 0x42e00400
	v_lshl_add_u64 v[88:89], v[4:5], 0, s[26:27]
	v_or_b32_e32 v4, 0xc00, v10
	v_ashrrev_i32_e32 v5, 31, v4
	v_lshl_add_u64 v[4:5], v[4:5], 2, s[84:85]
	v_ashrrev_i32_e32 v11, 31, v10
	v_lshl_add_u64 v[90:91], v[4:5], 0, s[8:9]
	v_lshl_add_u64 v[4:5], v[10:11], 2, s[84:85]
	v_lshl_add_u64 v[92:93], v[4:5], 0, s[8:9]
	v_or_b32_e32 v4, 0x400, v10
	v_ashrrev_i32_e32 v5, 31, v4
	v_lshl_add_u64 v[4:5], v[4:5], 2, s[84:85]
	v_lshl_add_u64 v[94:95], v[4:5], 0, s[8:9]
	v_or_b32_e32 v4, 0x480, v10
	v_ashrrev_i32_e32 v5, 31, v4
	v_lshl_add_u64 v[4:5], v[4:5], 2, s[84:85]
	v_lshl_add_u64 v[96:97], v[4:5], 0, s[8:9]
	v_or_b32_e32 v4, 0x500, v10
	v_ashrrev_i32_e32 v5, 31, v4
	v_lshl_add_u64 v[4:5], v[4:5], 2, s[84:85]
	v_lshl_add_u64 v[98:99], v[4:5], 0, s[8:9]
	v_or_b32_e32 v4, 0x580, v10
	v_ashrrev_i32_e32 v5, 31, v4
	v_lshl_add_u64 v[4:5], v[4:5], 2, s[84:85]
	v_lshl_add_u64 v[100:101], v[4:5], 0, s[8:9]
	v_or_b32_e32 v4, 0x800, v10
	v_ashrrev_i32_e32 v5, 31, v4
	v_lshl_add_u64 v[4:5], v[4:5], 2, s[84:85]
	v_lshl_add_u64 v[102:103], v[4:5], 0, s[8:9]
	v_or_b32_e32 v4, 0x880, v10
	v_ashrrev_i32_e32 v5, 31, v4
	v_lshl_add_u64 v[4:5], v[4:5], 2, s[84:85]
	v_or_b32_e32 v14, 0xd80, v10
	v_lshl_add_u64 v[104:105], v[4:5], 0, s[8:9]
	v_or_b32_e32 v4, 0x900, v10
	v_ashrrev_i32_e32 v15, 31, v14
	v_ashrrev_i32_e32 v5, 31, v4
	v_lshl_add_u64 v[14:15], v[14:15], 2, s[84:85]
	v_lshl_add_u64 v[4:5], v[4:5], 2, s[84:85]
	v_lshl_add_u64 v[80:81], v[14:15], 0, s[8:9]
	v_or_b32_e32 v14, 0xd00, v10
	v_lshl_add_u64 v[106:107], v[4:5], 0, s[8:9]
	v_or_b32_e32 v4, 0x980, v10
	v_ashrrev_i32_e32 v15, 31, v14
	v_ashrrev_i32_e32 v5, 31, v4
	v_mul_u32_u24_e32 v9, 0x140, v9
	v_mul_u32_u24_e32 v13, 0x140, v13
	v_mul_u32_u24_e32 v17, 0x140, v17
	s_movk_i32 s6, 0xff
	v_or_b32_e32 v21, 64, v73
	s_ashr_i32 s81, s80, 31
	v_lshl_add_u64 v[14:15], v[14:15], 2, s[84:85]
	v_lshl_add_u64 v[4:5], v[4:5], 2, s[84:85]
	s_mov_b32 s15, 0
	v_cmp_lt_u32_e64 s[6:7], s6, v0
	v_mov_b32_e32 v77, v71
	s_lshl_b32 s24, s80, 7
	s_lshl_b64 s[0:1], s[80:81], 16
	v_lshl_add_u64 v[82:83], v[14:15], 0, s[8:9]
	v_lshl_add_u64 v[108:109], v[4:5], 0, s[8:9]
	v_add_u32_e32 v118, v18, v9
	v_add_u32_e32 v119, v18, v13
	v_add_u32_e32 v120, v18, v17
	v_mov_b32_e32 v121, 0x358637bd
	s_mov_b32 s3, 0x800000
	v_lshlrev_b32_e32 v70, 1, v2
	v_lshlrev_b32_e32 v110, 1, v8
	v_lshlrev_b32_e32 v112, 1, v12
	v_lshlrev_b32_e32 v114, 1, v16
	v_add_u32_e32 v122, v19, v20
	v_add_u32_e32 v123, v75, v21
	v_add_u32_e32 v124, v19, v22
	v_add_u32_e32 v125, v19, v23
	v_add_u32_e32 v126, v19, v24
	s_mov_b32 s25, 0x42e00000
	s_mov_b32 s26, 0x42e01000
	s_mov_b32 s27, 0x42e02000
	s_mov_b32 s28, 0x42e03000
	s_mov_b32 s29, s2
	s_waitcnt vmcnt(0)
; __device__ __forceinline__ float hsum4(const f32x4 v) { return (v[0] + v[1]) + (v[2] + v[3]); }
; #define GAS __attribute__((address_space(1)))
; #define MFMA32(a, b, c) __builtin_amdgcn_mfma_f32_32x32x16_bf16((a), (b), (c), 0, 0, 0)
; DI void ret_kv_phase(LAS unsigned char* lds, const bf16* PROJ, float* KVB, const float* ssqsb, float* rsb, int bx, int G, int tid) {
;     ...
;     for (int unit = bx; unit < 2048; unit += G) {
;         const int n = unit & 63, hd = (unit >> 6) & 15, b = unit >> 10;
;         __syncthreads();
;         tile_st(KT, VSTR, kreg, tid); tile_st(VT, VSTR, vreg, tid);
;         if (tid < 256) rsb[((size_t)which * 32 + b * 16 + hd) * SEQ + 128 * n + (tid & 127)] = rsqrtf(hsum4(pp) * (1.0f / 128.0f) + EPSN);
;         __syncthreads();
;         { const int u2 = unit + G < 2048 ? unit + G : unit, n2 = u2 & 63, hd2 = (u2 >> 6) & 15, b2 = u2 >> 10; const size_t m2 = (size_t)b2 * SEQ + 128 * n2;
;           tile_ld(kreg, PROJ + m2 * INW + C_RK + 128 * hd2, INW, tid); tile_ld(vreg, PROJ + m2 * INW + C_RV + 128 * hd2, INW, tid);
;           pp = *(const GAS f32x4*)(ssqsb + ((m2 + (tid & 127)) * 32 + 16 * which + hd2) * 4); }
;         asm volatile("" ::: "memory");
;         f32x16 acc[2];
; #pragma unroll
;         for (int t = 0; t < 2; ++t)
; #pragma unroll
;             for (int i = 0; i < 16; ++i) acc[t][i] = 0.f;
; #pragma unroll
;         for (int ks = 0; ks < 8; ++ks) {
;             const bf16x8 a = tr_frag(VT, VSTR, 16 * ks, 32 * te, lane);
; #pragma unroll
;             for (int t = 0; t < 2; ++t) { const bf16x8 bb = tr_frag(KT, VSTR, 16 * ks, 32 * (td0 + t), lane); acc[t] = MFMA32(a, bb, acc[t]); }
;         }
	s_add_i32 s14, s29, s80
	s_cmpk_lt_i32 s14, 0x800
	s_cselect_b64 s[8:9], -1, 0
	s_and_b64 vcc, s[8:9], exec
	s_cselect_b32 s29, s14, s29
	s_ashr_i32 s8, s29, 10
	s_ashr_i32 s9, s8, 31
	s_lshl_b64 s[30:31], s[8:9], 13
	s_lshl_b32 s8, s29, 7
	s_and_b32 s8, s8, 0x1f80
	s_bfe_u32 s33, s29, 0x40006
	s_or_b32 s29, s30, s8
	s_mul_i32 s8, s31, 0x7000
	s_mul_hi_u32 s9, s29, 0x7000
	s_add_i32 s9, s9, s8
	s_mul_i32 s8, s29, 0x7000
	s_add_u32 s8, s42, s8
	s_addc_u32 s9, s43, s9
	s_lshl_b32 s30, s33, 8
	s_add_u32 s8, s8, s30
	s_addc_u32 s9, s9, 0
	v_lshl_add_u64 v[2:3], s[8:9], 0, v[70:71]
	v_lshl_add_u64 v[4:5], v[2:3], 0, s[16:17]
	v_mov_b32_e32 v111, v71
	v_lshl_add_u64 v[6:7], v[4:5], 0, v[110:111]
	v_mov_b32_e32 v113, v71
	v_lshl_add_u64 v[8:9], v[4:5], 0, v[112:113]
	global_load_dwordx4 v[184:187], v[6:7], off
	global_load_dwordx4 v[188:191], v[8:9], off
	v_add_co_u32_e64 v6, s[8:9], s23, v6
	v_mov_b32_e32 v115, v71
	s_nop 0
	v_addc_co_u32_e64 v7, s[8:9], 0, v7, s[8:9]
	v_lshl_add_u64 v[4:5], v[4:5], 0, v[114:115]
	v_lshl_add_u64 v[2:3], v[2:3], 0, s[18:19]
	global_load_dwordx4 v[192:195], v[6:7], off
	global_load_dwordx4 v[196:199], v[4:5], off
	v_lshl_add_u64 v[4:5], v[2:3], 0, v[110:111]
	v_lshl_add_u64 v[6:7], v[2:3], 0, v[112:113]
	global_load_dwordx4 v[200:203], v[4:5], off
	global_load_dwordx4 v[208:211], v[6:7], off
	v_add_co_u32_e64 v4, s[8:9], s23, v4
	v_lshl_add_u64 v[2:3], v[2:3], 0, v[114:115]
	s_nop 0
	v_addc_co_u32_e64 v5, s[8:9], 0, v5, s[8:9]
	global_load_dwordx4 v[212:215], v[4:5], off
	global_load_dwordx4 v[220:223], v[2:3], off
	v_mov_b32_e32 v3, s31
	v_or_b32_e32 v2, s29, v72
	v_lshlrev_b64 v[2:3], 5, v[2:3]
	v_or_b32_e32 v2, s33, v2
	v_or_b32_e32 v2, v2, v74
	v_lshl_add_u64 v[2:3], v[2:3], 4, s[10:11]
	global_load_dwordx4 v[216:219], v[2:3], off
	s_mov_b32 s29, s2
	s_branch .LBB0_400
.LBB0_399:
	s_or_b64 exec, exec, s[8:9]
	s_bfe_u32 s99, s29, 0x40006
	s_lshl_b32 s99, s99, 2
	s_getpc_b64 s[100:101]
	s_add_u32 s100, s100, _ZN3pg84LOGGE@rel32@lo+4
	s_addc_u32 s101, s101, _ZN3pg84LOGGE@rel32@hi+12
	s_load_dword s98, s[100:101], s99
	s_add_i32 s14, s29, s80
	s_add_i32 s30, s14, s80
	s_cmpk_lt_i32 s30, 0x800
	s_cselect_b32 s29, s30, s29
	s_cmpk_lt_i32 s14, 0x800
	s_cselect_b64 s[8:9], -1, 0
	s_and_b64 vcc, s[8:9], exec
	s_ashr_i32 s8, s29, 10
	s_ashr_i32 s9, s8, 31
	s_lshl_b64 s[30:31], s[8:9], 13
	s_lshl_b32 s8, s29, 7
	s_and_b32 s8, s8, 0x1f80
	s_bfe_u32 s33, s29, 0x40006
	s_or_b32 s29, s30, s8
	s_mul_i32 s8, s31, 0x7000
	s_mul_hi_u32 s9, s29, 0x7000
	s_add_i32 s9, s9, s8
	s_mul_i32 s8, s29, 0x7000
	s_add_u32 s8, s42, s8
	s_addc_u32 s9, s43, s9
	s_lshl_b32 s30, s33, 8
	s_add_u32 s8, s8, s30
	s_addc_u32 s9, s9, 0
	v_lshl_add_u64 v[2:3], s[8:9], 0, v[70:71]
	v_lshl_add_u64 v[4:5], v[2:3], 0, s[16:17]
	v_mov_b32_e32 v111, v71
	v_lshl_add_u64 v[6:7], v[4:5], 0, v[110:111]
	v_mov_b32_e32 v113, v71
	s_waitcnt lgkmcnt(0)
	s_barrier
	v_lshl_add_u64 v[8:9], v[4:5], 0, v[112:113]
	global_load_dwordx4 v[34:37], v[6:7], off
	global_load_dwordx4 v[38:41], v[8:9], off
	v_add_co_u32_e64 v6, s[8:9], s23, v6
	v_mov_b32_e32 v115, v71
	s_nop 0
	v_addc_co_u32_e64 v7, s[8:9], 0, v7, s[8:9]
	v_lshl_add_u64 v[4:5], v[4:5], 0, v[114:115]
	v_lshl_add_u64 v[2:3], v[2:3], 0, s[18:19]
	global_load_dwordx4 v[42:45], v[6:7], off
	global_load_dwordx4 v[46:49], v[4:5], off
	v_lshl_add_u64 v[4:5], v[2:3], 0, v[110:111]
	v_lshl_add_u64 v[6:7], v[2:3], 0, v[112:113]
	global_load_dwordx4 v[50:53], v[4:5], off
	global_load_dwordx4 v[54:57], v[6:7], off
	v_add_co_u32_e64 v4, s[8:9], s23, v4
	v_lshl_add_u64 v[2:3], v[2:3], 0, v[114:115]
	s_nop 0
	v_addc_co_u32_e64 v5, s[8:9], 0, v5, s[8:9]
	global_load_dwordx4 v[58:61], v[4:5], off
	global_load_dwordx4 v[66:69], v[2:3], off
	v_mov_b32_e32 v3, s31
	v_or_b32_e32 v2, s29, v72
	v_lshlrev_b64 v[2:3], 5, v[2:3]
	v_or_b32_e32 v2, s33, v2
	v_or_b32_e32 v2, v2, v74
	v_lshl_add_u64 v[2:3], v[2:3], 4, s[10:11]
	global_load_dwordx4 v[62:65], v[2:3], off
	ds_read_b64_tr_b16 v[2:3], v122 offset:40960
	ds_read_b64_tr_b16 v[4:5], v122 offset:43520
	v_add_u32_e32 v111, v75, v73
	ds_read_b64_tr_b16 v[6:7], v111
	ds_read_b64_tr_b16 v[8:9], v111 offset:2560
	ds_read_b64_tr_b16 v[128:129], v122 offset:46080
	ds_read_b64_tr_b16 v[130:131], v122 offset:48640
	ds_read_b64_tr_b16 v[132:133], v111 offset:5120
	ds_read_b64_tr_b16 v[136:137], v111 offset:38400
	s_waitcnt lgkmcnt(4)
	v_mfma_f32_32x32x16_bf16 v[18:33], v[2:5], v[6:9], 0
	ds_read_b64_tr_b16 v[6:7], v123
	ds_read_b64_tr_b16 v[8:9], v123 offset:2560
	ds_read_b64_tr_b16 v[138:139], v123 offset:5120
	ds_read_b64_tr_b16 v[142:143], v123 offset:38400
	ds_read_b64_tr_b16 v[134:135], v111 offset:7680
	ds_read_b64_tr_b16 v[144:145], v111 offset:10240
	ds_read_b64_tr_b16 v[146:147], v111 offset:12800
	ds_read_b64_tr_b16 v[148:149], v111 offset:15360
	s_add_i32 s22, s22, s24
	s_mov_b32 s29, s14
	s_waitcnt lgkmcnt(6)
	v_mfma_f32_32x32x16_bf16 v[2:17], v[2:5], v[6:9], 0
	s_waitcnt lgkmcnt(3)
	v_mfma_f32_32x32x16_bf16 v[18:33], v[128:131], v[132:135], v[18:33]
	ds_read_b64_tr_b16 v[140:141], v123 offset:7680
	ds_read_b64_tr_b16 v[132:133], v123 offset:10240
	ds_read_b64_tr_b16 v[134:135], v123 offset:12800
	ds_read_b64_tr_b16 v[152:153], v123 offset:15360
	s_waitcnt lgkmcnt(3)
	v_mfma_f32_32x32x16_bf16 v[2:17], v[128:131], v[138:141], v[2:17]
	ds_read_b64_tr_b16 v[128:129], v122 offset:51200
	ds_read_b64_tr_b16 v[130:131], v122 offset:53760
	ds_read_b64_tr_b16 v[138:139], v122 offset:56320
	ds_read_b64_tr_b16 v[140:141], v122 offset:58880
	s_waitcnt lgkmcnt(2)
; #define MFMA32(a, b, c) __builtin_amdgcn_mfma_f32_32x32x16_bf16((a), (b), (c), 0, 0, 0)
; DI int crow(int i, int h) { return (i & 3) + 8 * (i >> 2) + 4 * h; }
; DI void ret_kv_phase(LAS unsigned char* lds, const bf16* PROJ, float* KVB, const float* ssqsb, float* rsb, int bx, int G, int tid) {
;     ...
; #pragma unroll
;         for (int ks = 0; ks < 8; ++ks) {
;             const bf16x8 a = tr_frag(VT, VSTR, 16 * ks, 32 * te, lane);
; #pragma unroll
;             for (int t = 0; t < 2; ++t) { const bf16x8 bb = tr_frag(KT, VSTR, 16 * ks, 32 * (td0 + t), lane); acc[t] = MFMA32(a, bb, acc[t]); }
;         }
;         const float sc = __expf(127.0f * LOGG[hd]);
;         float* o = KVB + (size_t)unit * 16384;
; #pragma unroll
;         for (int t = 0; t < 2; ++t)
; #pragma unroll
;             for (int i = 0; i < 16; ++i) o[(32 * te + crow(i, h)) * 128 + 32 * (td0 + t) + r] = acc[t][i] * sc;
;     }
	v_mfma_f32_32x32x16_bf16 v[18:33], v[128:131], v[144:147], v[18:33]
	v_mfma_f32_32x32x16_bf16 v[2:17], v[128:131], v[132:135], v[2:17]
	ds_read_b64_tr_b16 v[150:151], v111 offset:17920
	ds_read_b64_tr_b16 v[128:129], v111 offset:20480
	ds_read_b64_tr_b16 v[130:131], v111 offset:23040
	ds_read_b64_tr_b16 v[144:145], v111 offset:25600
	s_waitcnt lgkmcnt(3)
	v_mfma_f32_32x32x16_bf16 v[18:33], v[138:141], v[148:151], v[18:33]
	ds_read_b64_tr_b16 v[154:155], v123 offset:17920
	ds_read_b64_tr_b16 v[146:147], v123 offset:20480
	ds_read_b64_tr_b16 v[148:149], v123 offset:23040
	ds_read_b64_tr_b16 v[150:151], v123 offset:25600
	s_waitcnt lgkmcnt(3)
	v_mfma_f32_32x32x16_bf16 v[2:17], v[138:141], v[152:155], v[2:17]
	ds_read_b64_tr_b16 v[138:139], v122 offset:61440
	ds_read_b64_tr_b16 v[140:141], v122 offset:64000
	ds_read_b64_tr_b16 v[132:133], v111 offset:33280
	ds_read_b64_tr_b16 v[134:135], v111 offset:35840
	s_waitcnt lgkmcnt(2)
	v_mfma_f32_32x32x16_bf16 v[18:33], v[138:141], v[128:131], v[18:33]
	v_mfma_f32_32x32x16_bf16 v[2:17], v[138:141], v[146:149], v[2:17]
	ds_read_b64_tr_b16 v[154:155], v124 offset:40960
	ds_read_b64_tr_b16 v[156:157], v124 offset:43520
	ds_read_b64_tr_b16 v[146:147], v111 offset:28160
	ds_read_b64_tr_b16 v[158:159], v123 offset:30720
	ds_read_b64_tr_b16 v[130:131], v111 offset:30720
	ds_read_b64_tr_b16 v[160:161], v123 offset:33280
	ds_read_b64_tr_b16 v[140:141], v123 offset:35840
	ds_read_b64_tr_b16 v[152:153], v123 offset:28160
	v_lshl_add_u64 v[116:117], v[92:93], 0, s[20:21]
	v_lshl_add_u64 v[92:93], v[92:93], 0, s[0:1]
	s_waitcnt lgkmcnt(5)
	v_mfma_f32_32x32x16_bf16 v[18:33], v[154:157], v[144:147], v[18:33]
	s_waitcnt lgkmcnt(0)
	v_mfma_f32_32x32x16_bf16 v[2:17], v[154:157], v[150:153], v[2:17]
	ds_read_b64_tr_b16 v[144:145], v125 offset:40960
	ds_read_b64_tr_b16 v[146:147], v125 offset:43520
	ds_read_b64_tr_b16 v[148:149], v126 offset:40960
	ds_read_b64_tr_b16 v[150:151], v126 offset:43520
	v_mov_b32_e32 v111, s98
	v_mul_f32_e32 v111, 0x42fe0000, v111
	s_waitcnt lgkmcnt(2)
	v_mfma_f32_32x32x16_bf16 v[18:33], v[144:147], v[130:133], v[18:33]
	v_mul_f32_e32 v111, 0x3fb8aa3b, v111
	v_exp_f32_e32 v111, v111
	s_waitcnt lgkmcnt(0)
	v_mfma_f32_32x32x16_bf16 v[18:33], v[148:151], v[134:137], v[18:33]
	v_mfma_f32_32x32x16_bf16 v[2:17], v[144:147], v[158:161], v[2:17]
	s_nop 10
	v_mul_f32_e32 v18, v18, v111
	global_store_dword v[116:117], v18, off
	v_mul_f32_e32 v113, v19, v111
	v_lshl_add_u64 v[18:19], v[88:89], 0, s[20:21]
	v_mul_f32_e32 v20, v20, v111
	global_store_dword v[18:19], v20, off
	v_mul_f32_e32 v20, v21, v111
	global_store_dword v[18:19], v113, off offset:-512
	global_store_dword v[18:19], v20, off offset:512
	v_mul_f32_e32 v20, v22, v111
	v_lshl_add_u64 v[18:19], v[94:95], 0, s[20:21]
	global_store_dword v[18:19], v20, off
	v_mul_f32_e32 v20, v23, v111
	v_lshl_add_u64 v[18:19], v[96:97], 0, s[20:21]
	global_store_dword v[18:19], v20, off
	v_mul_f32_e32 v20, v24, v111
	v_lshl_add_u64 v[18:19], v[98:99], 0, s[20:21]
	global_store_dword v[18:19], v20, off
	v_mul_f32_e32 v20, v25, v111
	v_lshl_add_u64 v[18:19], v[100:101], 0, s[20:21]
	v_mfma_f32_32x32x16_bf16 v[2:17], v[148:151], v[140:143], v[2:17]
	global_store_dword v[18:19], v20, off
	v_mul_f32_e32 v20, v26, v111
	v_lshl_add_u64 v[18:19], v[102:103], 0, s[20:21]
	global_store_dword v[18:19], v20, off
	v_mul_f32_e32 v20, v27, v111
	v_lshl_add_u64 v[18:19], v[104:105], 0, s[20:21]
	global_store_dword v[18:19], v20, off
	v_mul_f32_e32 v20, v28, v111
	v_lshl_add_u64 v[18:19], v[106:107], 0, s[20:21]
	global_store_dword v[18:19], v20, off
	v_mul_f32_e32 v20, v29, v111
	v_lshl_add_u64 v[18:19], v[108:109], 0, s[20:21]
	global_store_dword v[18:19], v20, off
	v_mul_f32_e32 v20, v30, v111
	v_lshl_add_u64 v[18:19], v[90:91], 0, s[20:21]
	global_store_dword v[18:19], v20, off
	v_mul_f32_e32 v20, v31, v111
	v_lshl_add_u64 v[18:19], v[86:87], 0, s[20:21]
	global_store_dword v[18:19], v20, off
	v_mul_f32_e32 v20, v32, v111
	v_lshl_add_u64 v[18:19], v[82:83], 0, s[20:21]
	global_store_dword v[18:19], v20, off
	v_mul_f32_e32 v20, v33, v111
	v_lshl_add_u64 v[18:19], v[80:81], 0, s[20:21]
	global_store_dword v[18:19], v20, off
	v_mul_f32_e32 v2, v2, v111
	v_lshl_add_u64 v[18:19], v[84:85], 0, s[20:21]
	global_store_dword v[18:19], v2, off
	v_mul_f32_e32 v20, v3, v111
	v_lshl_add_u64 v[2:3], v[78:79], 0, s[20:21]
	v_add_co_u32_e64 v18, s[8:9], s25, v2
	v_mul_f32_e32 v4, v4, v111
	s_nop 0
	v_addc_co_u32_e64 v19, s[8:9], 0, v3, s[8:9]
	global_store_dword v[18:19], v4, off offset:1152
	v_mul_f32_e32 v4, v5, v111
	global_store_dword v[18:19], v4, off offset:1664
	v_add_co_u32_e64 v4, s[8:9], s26, v2
	v_mul_f32_e32 v6, v6, v111
	s_nop 0
	v_addc_co_u32_e64 v5, s[8:9], 0, v3, s[8:9]
	global_store_dword v[4:5], v6, off offset:128
	v_mul_f32_e32 v6, v7, v111
	global_store_dword v[4:5], v6, off offset:640
	v_mul_f32_e32 v6, v8, v111
	global_store_dword v[4:5], v6, off offset:1152
	v_mul_f32_e32 v6, v9, v111
	global_store_dword v[4:5], v6, off offset:1664
	v_add_co_u32_e64 v4, s[8:9], s27, v2
	v_mul_f32_e32 v6, v10, v111
	s_nop 0
	v_addc_co_u32_e64 v5, s[8:9], 0, v3, s[8:9]
	global_store_dword v[4:5], v6, off offset:128
	v_mul_f32_e32 v6, v11, v111
	global_store_dword v[4:5], v6, off offset:640
	v_mul_f32_e32 v6, v12, v111
	global_store_dword v[4:5], v6, off offset:1152
	v_mul_f32_e32 v6, v13, v111
	v_add_co_u32_e64 v2, s[8:9], s28, v2
	global_store_dword v[4:5], v6, off offset:1664
	v_mul_f32_e32 v4, v14, v111
	v_addc_co_u32_e64 v3, s[8:9], 0, v3, s[8:9]
	global_store_dword v[2:3], v4, off offset:128
	v_mul_f32_e32 v4, v15, v111
	global_store_dword v[2:3], v4, off offset:640
	v_mul_f32_e32 v4, v16, v111
	global_store_dword v[2:3], v4, off offset:1152
	v_mul_f32_e32 v4, v17, v111
	v_lshl_add_u64 v[78:79], v[78:79], 0, s[0:1]
	v_lshl_add_u64 v[80:81], v[80:81], 0, s[0:1]
	v_lshl_add_u64 v[82:83], v[82:83], 0, s[0:1]
	v_lshl_add_u64 v[84:85], v[84:85], 0, s[0:1]
	v_lshl_add_u64 v[86:87], v[86:87], 0, s[0:1]
	v_lshl_add_u64 v[88:89], v[88:89], 0, s[0:1]
	v_lshl_add_u64 v[90:91], v[90:91], 0, s[0:1]
	v_lshl_add_u64 v[94:95], v[94:95], 0, s[0:1]
	v_lshl_add_u64 v[96:97], v[96:97], 0, s[0:1]
	v_lshl_add_u64 v[98:99], v[98:99], 0, s[0:1]
	v_lshl_add_u64 v[100:101], v[100:101], 0, s[0:1]
	v_lshl_add_u64 v[102:103], v[102:103], 0, s[0:1]
	v_lshl_add_u64 v[104:105], v[104:105], 0, s[0:1]
	v_lshl_add_u64 v[106:107], v[106:107], 0, s[0:1]
	v_lshl_add_u64 v[108:109], v[108:109], 0, s[0:1]
	global_store_dword v[18:19], v20, off offset:640
	global_store_dword v[2:3], v4, off offset:1664
	s_cbranch_vccz .LBB0_404
; __device__ __forceinline__ float hsum4(const f32x4 v) { return (v[0] + v[1]) + (v[2] + v[3]); }
; #define GAS __attribute__((address_space(1)))
; #define MFMA32(a, b, c) __builtin_amdgcn_mfma_f32_32x32x16_bf16((a), (b), (c), 0, 0, 0)
; DI void ret_kv_phase(LAS unsigned char* lds, const bf16* PROJ, float* KVB, const float* ssqsb, float* rsb, int bx, int G, int tid) {
;     ...
;         __syncthreads();
;         tile_st(KT, VSTR, kreg, tid); tile_st(VT, VSTR, vreg, tid);
;         if (tid < 256) rsb[((size_t)which * 32 + b * 16 + hd) * SEQ + 128 * n + (tid & 127)] = rsqrtf(hsum4(pp) * (1.0f / 128.0f) + EPSN);
;         __syncthreads();
;         { const int u2 = unit + G < 2048 ? unit + G : unit, n2 = u2 & 63, hd2 = (u2 >> 6) & 15, b2 = u2 >> 10; const size_t m2 = (size_t)b2 * SEQ + 128 * n2;
;           tile_ld(kreg, PROJ + m2 * INW + C_RK + 128 * hd2, INW, tid); tile_ld(vreg, PROJ + m2 * INW + C_RV + 128 * hd2, INW, tid);
;           pp = *(const GAS f32x4*)(ssqsb + ((m2 + (tid & 127)) * 32 + 16 * which + hd2) * 4); }
;         asm volatile("" ::: "memory");
;     ...
; #pragma unroll
;         for (int ks = 0; ks < 8; ++ks) {
;             const bf16x8 a = tr_frag(VT, VSTR, 16 * ks, 32 * te, lane);
; #pragma unroll
;             for (int t = 0; t < 2; ++t) { const bf16x8 bb = tr_frag(KT, VSTR, 16 * ks, 32 * (td0 + t), lane); acc[t] = MFMA32(a, bb, acc[t]); }
;         }
.Lp2_hdrB:
	s_bfe_u32 s14, s29, 0x40006
	v_mov_b64_e32 v[116:117], s[14:15]
	s_waitcnt vmcnt(41) lgkmcnt(0)
	s_barrier
	ds_write_b128 v118, v[184:187]
	ds_write_b128 v119, v[188:191]
	ds_write_b128 v118, v[192:195] offset:20480
	ds_write_b128 v120, v[196:199]
	ds_write_b128 v118, v[200:203] offset:40960
	ds_write_b128 v119, v[208:211] offset:40960
	ds_write_b128 v118, v[212:215] offset:61440
	ds_write_b128 v120, v[220:223] offset:40960
	s_and_saveexec_b64 s[8:9], s[6:7]
	s_xor_b64 s[8:9], exec, s[8:9]
	v_mov_b64_e32 v[116:117], s[14:15]
	s_andn2_saveexec_b64 s[8:9], s[8:9]
	s_cbranch_execz .Lp2_bodyB
	v_mov_b32_e32 v2, v217
	v_mov_b32_e32 v3, v218
	v_mov_b32_e32 v217, v219
	v_pk_add_f32 v[2:3], v[2:3], v[216:217]
	s_ashr_i32 s30, s29, 6
	v_add_f32_e32 v2, v2, v3
	v_fmamk_f32 v2, v2, 0x3c000000, v121
	v_mul_f32_e32 v3, 0x4b800000, v2
	v_cmp_gt_f32_e32 vcc, s3, v2
	s_and_b32 s30, s30, -16
	s_ashr_i32 s31, s30, 31
	v_cndmask_b32_e32 v2, v2, v3, vcc
	v_rsq_f32_e32 v2, v2
	v_lshlrev_b32_e32 v4, 2, v72
	v_mov_b32_e32 v5, v71
	v_mul_f32_e32 v3, 0x45800000, v2
	v_cndmask_b32_e32 v6, v2, v3, vcc
	v_lshl_add_u64 v[2:3], s[30:31], 0, v[76:77]
	v_or_b32_e32 v2, s14, v2
	s_and_b32 s14, s22, 0x1f80
	v_lshlrev_b64 v[2:3], 15, v[2:3]
	v_lshl_add_u64 v[2:3], s[12:13], 0, v[2:3]
	s_lshl_b32 s14, s14, 2
	v_lshl_add_u64 v[2:3], v[2:3], 0, s[14:15]
	v_lshl_add_u64 v[2:3], v[2:3], 0, v[4:5]
	global_store_dword v[2:3], v6, off
	s_branch .Lp2_bodyB
.Lp2_bodyB:
	s_or_b64 exec, exec, s[8:9]
	s_bfe_u32 s99, s29, 0x40006
	s_lshl_b32 s99, s99, 2
	s_getpc_b64 s[100:101]
	s_add_u32 s100, s100, _ZN3pg84LOGGE@rel32@lo+4
	s_addc_u32 s101, s101, _ZN3pg84LOGGE@rel32@hi+12
	s_load_dword s98, s[100:101], s99
	s_add_i32 s14, s29, s80
	s_add_i32 s30, s14, s80
	s_cmpk_lt_i32 s30, 0x800
	s_cselect_b32 s29, s30, s29
	s_cmpk_lt_i32 s14, 0x800
	s_cselect_b64 s[8:9], -1, 0
	s_and_b64 vcc, s[8:9], exec
	s_ashr_i32 s8, s29, 10
	s_ashr_i32 s9, s8, 31
	s_lshl_b64 s[30:31], s[8:9], 13
	s_lshl_b32 s8, s29, 7
	s_and_b32 s8, s8, 0x1f80
	s_bfe_u32 s33, s29, 0x40006
	s_or_b32 s29, s30, s8
	s_mul_i32 s8, s31, 0x7000
	s_mul_hi_u32 s9, s29, 0x7000
	s_add_i32 s9, s9, s8
	s_mul_i32 s8, s29, 0x7000
	s_add_u32 s8, s42, s8
	s_addc_u32 s9, s43, s9
	s_lshl_b32 s30, s33, 8
	s_add_u32 s8, s8, s30
	s_addc_u32 s9, s9, 0
	v_lshl_add_u64 v[2:3], s[8:9], 0, v[70:71]
	v_lshl_add_u64 v[4:5], v[2:3], 0, s[16:17]
	v_mov_b32_e32 v111, v71
	v_lshl_add_u64 v[6:7], v[4:5], 0, v[110:111]
	v_mov_b32_e32 v113, v71
	s_waitcnt lgkmcnt(0)
	s_barrier
	v_lshl_add_u64 v[8:9], v[4:5], 0, v[112:113]
	global_load_dwordx4 v[184:187], v[6:7], off
	global_load_dwordx4 v[188:191], v[8:9], off
	v_add_co_u32_e64 v6, s[8:9], s23, v6
	v_mov_b32_e32 v115, v71
	s_nop 0
	v_addc_co_u32_e64 v7, s[8:9], 0, v7, s[8:9]
	v_lshl_add_u64 v[4:5], v[4:5], 0, v[114:115]
	v_lshl_add_u64 v[2:3], v[2:3], 0, s[18:19]
	global_load_dwordx4 v[192:195], v[6:7], off
	global_load_dwordx4 v[196:199], v[4:5], off
	v_lshl_add_u64 v[4:5], v[2:3], 0, v[110:111]
	v_lshl_add_u64 v[6:7], v[2:3], 0, v[112:113]
	global_load_dwordx4 v[200:203], v[4:5], off
	global_load_dwordx4 v[208:211], v[6:7], off
	v_add_co_u32_e64 v4, s[8:9], s23, v4
	v_lshl_add_u64 v[2:3], v[2:3], 0, v[114:115]
	s_nop 0
	v_addc_co_u32_e64 v5, s[8:9], 0, v5, s[8:9]
	global_load_dwordx4 v[212:215], v[4:5], off
	global_load_dwordx4 v[220:223], v[2:3], off
	v_mov_b32_e32 v3, s31
	v_or_b32_e32 v2, s29, v72
	v_lshlrev_b64 v[2:3], 5, v[2:3]
	v_or_b32_e32 v2, s33, v2
	v_or_b32_e32 v2, v2, v74
	v_lshl_add_u64 v[2:3], v[2:3], 4, s[10:11]
	global_load_dwordx4 v[216:219], v[2:3], off
	ds_read_b64_tr_b16 v[2:3], v122 offset:40960
	ds_read_b64_tr_b16 v[4:5], v122 offset:43520
	v_add_u32_e32 v111, v75, v73
	ds_read_b64_tr_b16 v[6:7], v111
	ds_read_b64_tr_b16 v[8:9], v111 offset:2560
	ds_read_b64_tr_b16 v[128:129], v122 offset:46080
	ds_read_b64_tr_b16 v[130:131], v122 offset:48640
	ds_read_b64_tr_b16 v[132:133], v111 offset:5120
	ds_read_b64_tr_b16 v[136:137], v111 offset:38400
	s_waitcnt lgkmcnt(4)
	v_mfma_f32_32x32x16_bf16 v[18:33], v[2:5], v[6:9], 0
	ds_read_b64_tr_b16 v[6:7], v123
	ds_read_b64_tr_b16 v[8:9], v123 offset:2560
	ds_read_b64_tr_b16 v[138:139], v123 offset:5120
	ds_read_b64_tr_b16 v[142:143], v123 offset:38400
	ds_read_b64_tr_b16 v[134:135], v111 offset:7680
	ds_read_b64_tr_b16 v[144:145], v111 offset:10240
	ds_read_b64_tr_b16 v[146:147], v111 offset:12800
	ds_read_b64_tr_b16 v[148:149], v111 offset:15360
	s_add_i32 s22, s22, s24
	s_mov_b32 s29, s14
	s_waitcnt lgkmcnt(6)
	v_mfma_f32_32x32x16_bf16 v[2:17], v[2:5], v[6:9], 0
	s_waitcnt lgkmcnt(3)
	v_mfma_f32_32x32x16_bf16 v[18:33], v[128:131], v[132:135], v[18:33]
	ds_read_b64_tr_b16 v[140:141], v123 offset:7680
	ds_read_b64_tr_b16 v[132:133], v123 offset:10240
	ds_read_b64_tr_b16 v[134:135], v123 offset:12800
	ds_read_b64_tr_b16 v[152:153], v123 offset:15360
	s_waitcnt lgkmcnt(3)
	v_mfma_f32_32x32x16_bf16 v[2:17], v[128:131], v[138:141], v[2:17]
	ds_read_b64_tr_b16 v[128:129], v122 offset:51200
	ds_read_b64_tr_b16 v[130:131], v122 offset:53760
	ds_read_b64_tr_b16 v[138:139], v122 offset:56320
	ds_read_b64_tr_b16 v[140:141], v122 offset:58880
	s_waitcnt lgkmcnt(2)
	v_mfma_f32_32x32x16_bf16 v[18:33], v[128:131], v[144:147], v[18:33]
	v_mfma_f32_32x32x16_bf16 v[2:17], v[128:131], v[132:135], v[2:17]
	ds_read_b64_tr_b16 v[150:151], v111 offset:17920
	ds_read_b64_tr_b16 v[128:129], v111 offset:20480
	ds_read_b64_tr_b16 v[130:131], v111 offset:23040
	ds_read_b64_tr_b16 v[144:145], v111 offset:25600
	s_waitcnt lgkmcnt(3)
; #define MFMA32(a, b, c) __builtin_amdgcn_mfma_f32_32x32x16_bf16((a), (b), (c), 0, 0, 0)
; DI int crow(int i, int h) { return (i & 3) + 8 * (i >> 2) + 4 * h; }
; DI void ret_kv_phase(LAS unsigned char* lds, const bf16* PROJ, float* KVB, const float* ssqsb, float* rsb, int bx, int G, int tid) {
;     ...
; #pragma unroll
;         for (int ks = 0; ks < 8; ++ks) {
;             const bf16x8 a = tr_frag(VT, VSTR, 16 * ks, 32 * te, lane);
; #pragma unroll
;             for (int t = 0; t < 2; ++t) { const bf16x8 bb = tr_frag(KT, VSTR, 16 * ks, 32 * (td0 + t), lane); acc[t] = MFMA32(a, bb, acc[t]); }
;         }
;         const float sc = __expf(127.0f * LOGG[hd]);
;         float* o = KVB + (size_t)unit * 16384;
; #pragma unroll
;         for (int t = 0; t < 2; ++t)
; #pragma unroll
;             for (int i = 0; i < 16; ++i) o[(32 * te + crow(i, h)) * 128 + 32 * (td0 + t) + r] = acc[t][i] * sc;
;     }
	v_mfma_f32_32x32x16_bf16 v[18:33], v[138:141], v[148:151], v[18:33]
	ds_read_b64_tr_b16 v[154:155], v123 offset:17920
	ds_read_b64_tr_b16 v[146:147], v123 offset:20480
	ds_read_b64_tr_b16 v[148:149], v123 offset:23040
	ds_read_b64_tr_b16 v[150:151], v123 offset:25600
	s_waitcnt lgkmcnt(3)
	v_mfma_f32_32x32x16_bf16 v[2:17], v[138:141], v[152:155], v[2:17]
	ds_read_b64_tr_b16 v[138:139], v122 offset:61440
	ds_read_b64_tr_b16 v[140:141], v122 offset:64000
	ds_read_b64_tr_b16 v[132:133], v111 offset:33280
	ds_read_b64_tr_b16 v[134:135], v111 offset:35840
	s_waitcnt lgkmcnt(2)
	v_mfma_f32_32x32x16_bf16 v[18:33], v[138:141], v[128:131], v[18:33]
	v_mfma_f32_32x32x16_bf16 v[2:17], v[138:141], v[146:149], v[2:17]
	ds_read_b64_tr_b16 v[154:155], v124 offset:40960
	ds_read_b64_tr_b16 v[156:157], v124 offset:43520
	ds_read_b64_tr_b16 v[146:147], v111 offset:28160
	ds_read_b64_tr_b16 v[158:159], v123 offset:30720
	ds_read_b64_tr_b16 v[130:131], v111 offset:30720
	ds_read_b64_tr_b16 v[160:161], v123 offset:33280
	ds_read_b64_tr_b16 v[140:141], v123 offset:35840
	ds_read_b64_tr_b16 v[152:153], v123 offset:28160
	v_lshl_add_u64 v[116:117], v[92:93], 0, s[20:21]
	v_lshl_add_u64 v[92:93], v[92:93], 0, s[0:1]
	s_waitcnt lgkmcnt(5)
	v_mfma_f32_32x32x16_bf16 v[18:33], v[154:157], v[144:147], v[18:33]
	s_waitcnt lgkmcnt(0)
	v_mfma_f32_32x32x16_bf16 v[2:17], v[154:157], v[150:153], v[2:17]
	ds_read_b64_tr_b16 v[144:145], v125 offset:40960
	ds_read_b64_tr_b16 v[146:147], v125 offset:43520
	ds_read_b64_tr_b16 v[148:149], v126 offset:40960
	ds_read_b64_tr_b16 v[150:151], v126 offset:43520
	v_mov_b32_e32 v111, s98
	v_mul_f32_e32 v111, 0x42fe0000, v111
	s_waitcnt lgkmcnt(2)
	v_mfma_f32_32x32x16_bf16 v[18:33], v[144:147], v[130:133], v[18:33]
	v_mul_f32_e32 v111, 0x3fb8aa3b, v111
	v_exp_f32_e32 v111, v111
	s_waitcnt lgkmcnt(0)
	v_mfma_f32_32x32x16_bf16 v[18:33], v[148:151], v[134:137], v[18:33]
	v_mfma_f32_32x32x16_bf16 v[2:17], v[144:147], v[158:161], v[2:17]
	s_nop 10
	v_mul_f32_e32 v18, v18, v111
	global_store_dword v[116:117], v18, off
	v_mul_f32_e32 v113, v19, v111
	v_lshl_add_u64 v[18:19], v[88:89], 0, s[20:21]
	v_mul_f32_e32 v20, v20, v111
	global_store_dword v[18:19], v20, off
	v_mul_f32_e32 v20, v21, v111
	global_store_dword v[18:19], v113, off offset:-512
	global_store_dword v[18:19], v20, off offset:512
	v_mul_f32_e32 v20, v22, v111
	v_lshl_add_u64 v[18:19], v[94:95], 0, s[20:21]
	global_store_dword v[18:19], v20, off
	v_mul_f32_e32 v20, v23, v111
	v_lshl_add_u64 v[18:19], v[96:97], 0, s[20:21]
	global_store_dword v[18:19], v20, off
	v_mul_f32_e32 v20, v24, v111
	v_lshl_add_u64 v[18:19], v[98:99], 0, s[20:21]
	global_store_dword v[18:19], v20, off
	v_mul_f32_e32 v20, v25, v111
	v_lshl_add_u64 v[18:19], v[100:101], 0, s[20:21]
	v_mfma_f32_32x32x16_bf16 v[2:17], v[148:151], v[140:143], v[2:17]
	global_store_dword v[18:19], v20, off
	v_mul_f32_e32 v20, v26, v111
	v_lshl_add_u64 v[18:19], v[102:103], 0, s[20:21]
	global_store_dword v[18:19], v20, off
	v_mul_f32_e32 v20, v27, v111
	v_lshl_add_u64 v[18:19], v[104:105], 0, s[20:21]
	global_store_dword v[18:19], v20, off
	v_mul_f32_e32 v20, v28, v111
	v_lshl_add_u64 v[18:19], v[106:107], 0, s[20:21]
	global_store_dword v[18:19], v20, off
	v_mul_f32_e32 v20, v29, v111
	v_lshl_add_u64 v[18:19], v[108:109], 0, s[20:21]
	global_store_dword v[18:19], v20, off
	v_mul_f32_e32 v20, v30, v111
	v_lshl_add_u64 v[18:19], v[90:91], 0, s[20:21]
	global_store_dword v[18:19], v20, off
	v_mul_f32_e32 v20, v31, v111
	v_lshl_add_u64 v[18:19], v[86:87], 0, s[20:21]
	global_store_dword v[18:19], v20, off
	v_mul_f32_e32 v20, v32, v111
	v_lshl_add_u64 v[18:19], v[82:83], 0, s[20:21]
	global_store_dword v[18:19], v20, off
	v_mul_f32_e32 v20, v33, v111
	v_lshl_add_u64 v[18:19], v[80:81], 0, s[20:21]
	global_store_dword v[18:19], v20, off
	v_mul_f32_e32 v2, v2, v111
	v_lshl_add_u64 v[18:19], v[84:85], 0, s[20:21]
	global_store_dword v[18:19], v2, off
	v_mul_f32_e32 v20, v3, v111
	v_lshl_add_u64 v[2:3], v[78:79], 0, s[20:21]
	v_add_co_u32_e64 v18, s[8:9], s25, v2
	v_mul_f32_e32 v4, v4, v111
	s_nop 0
	v_addc_co_u32_e64 v19, s[8:9], 0, v3, s[8:9]
	global_store_dword v[18:19], v4, off offset:1152
	v_mul_f32_e32 v4, v5, v111
	global_store_dword v[18:19], v4, off offset:1664
	v_add_co_u32_e64 v4, s[8:9], s26, v2
	v_mul_f32_e32 v6, v6, v111
	s_nop 0
	v_addc_co_u32_e64 v5, s[8:9], 0, v3, s[8:9]
	global_store_dword v[4:5], v6, off offset:128
	v_mul_f32_e32 v6, v7, v111
	global_store_dword v[4:5], v6, off offset:640
	v_mul_f32_e32 v6, v8, v111
	global_store_dword v[4:5], v6, off offset:1152
	v_mul_f32_e32 v6, v9, v111
	global_store_dword v[4:5], v6, off offset:1664
	v_add_co_u32_e64 v4, s[8:9], s27, v2
	v_mul_f32_e32 v6, v10, v111
	s_nop 0
	v_addc_co_u32_e64 v5, s[8:9], 0, v3, s[8:9]
	global_store_dword v[4:5], v6, off offset:128
	v_mul_f32_e32 v6, v11, v111
	global_store_dword v[4:5], v6, off offset:640
	v_mul_f32_e32 v6, v12, v111
	global_store_dword v[4:5], v6, off offset:1152
	v_mul_f32_e32 v6, v13, v111
	v_add_co_u32_e64 v2, s[8:9], s28, v2
	global_store_dword v[4:5], v6, off offset:1664
	v_mul_f32_e32 v4, v14, v111
	v_addc_co_u32_e64 v3, s[8:9], 0, v3, s[8:9]
	global_store_dword v[2:3], v4, off offset:128
	v_mul_f32_e32 v4, v15, v111
	global_store_dword v[2:3], v4, off offset:640
	v_mul_f32_e32 v4, v16, v111
	global_store_dword v[2:3], v4, off offset:1152
	v_mul_f32_e32 v4, v17, v111
	v_lshl_add_u64 v[78:79], v[78:79], 0, s[0:1]
	v_lshl_add_u64 v[80:81], v[80:81], 0, s[0:1]
	v_lshl_add_u64 v[82:83], v[82:83], 0, s[0:1]
	v_lshl_add_u64 v[84:85], v[84:85], 0, s[0:1]
	v_lshl_add_u64 v[86:87], v[86:87], 0, s[0:1]
	v_lshl_add_u64 v[88:89], v[88:89], 0, s[0:1]
	v_lshl_add_u64 v[90:91], v[90:91], 0, s[0:1]
	v_lshl_add_u64 v[94:95], v[94:95], 0, s[0:1]
	v_lshl_add_u64 v[96:97], v[96:97], 0, s[0:1]
	v_lshl_add_u64 v[98:99], v[98:99], 0, s[0:1]
	v_lshl_add_u64 v[100:101], v[100:101], 0, s[0:1]
	v_lshl_add_u64 v[102:103], v[102:103], 0, s[0:1]
	v_lshl_add_u64 v[104:105], v[104:105], 0, s[0:1]
	v_lshl_add_u64 v[106:107], v[106:107], 0, s[0:1]
	v_lshl_add_u64 v[108:109], v[108:109], 0, s[0:1]
	global_store_dword v[18:19], v20, off offset:640
	global_store_dword v[2:3], v4, off offset:1664
	s_cbranch_vccz .LBB0_404
; __device__ __forceinline__ float hsum4(const f32x4 v) { return (v[0] + v[1]) + (v[2] + v[3]); }
; DI void ret_kv_phase(LAS unsigned char* lds, const bf16* PROJ, float* KVB, const float* ssqsb, float* rsb, int bx, int G, int tid) {
;     ...
;         __syncthreads();
;         tile_st(KT, VSTR, kreg, tid); tile_st(VT, VSTR, vreg, tid);
;         if (tid < 256) rsb[((size_t)which * 32 + b * 16 + hd) * SEQ + 128 * n + (tid & 127)] = rsqrtf(hsum4(pp) * (1.0f / 128.0f) + EPSN);
.LBB0_400:
	s_bfe_u32 s14, s29, 0x40006
	v_mov_b64_e32 v[116:117], s[14:15]
	s_waitcnt vmcnt(41) lgkmcnt(0)
	s_barrier
	ds_write_b128 v118, v[34:37]
	ds_write_b128 v119, v[38:41]
	ds_write_b128 v118, v[42:45] offset:20480
	ds_write_b128 v120, v[46:49]
	ds_write_b128 v118, v[50:53] offset:40960
	ds_write_b128 v119, v[54:57] offset:40960
	ds_write_b128 v118, v[58:61] offset:61440
	ds_write_b128 v120, v[66:69] offset:40960
	s_and_saveexec_b64 s[8:9], s[6:7]
	s_xor_b64 s[8:9], exec, s[8:9]
	v_mov_b64_e32 v[116:117], s[14:15]
	s_andn2_saveexec_b64 s[8:9], s[8:9]
	s_cbranch_execz .LBB0_399
	v_mov_b32_e32 v2, v63
	v_mov_b32_e32 v3, v64
	v_mov_b32_e32 v63, v65
	v_pk_add_f32 v[2:3], v[2:3], v[62:63]
	s_ashr_i32 s30, s29, 6
	v_add_f32_e32 v2, v2, v3
	v_fmamk_f32 v2, v2, 0x3c000000, v121
	v_mul_f32_e32 v3, 0x4b800000, v2
	v_cmp_gt_f32_e32 vcc, s3, v2
	s_and_b32 s30, s30, -16
	s_ashr_i32 s31, s30, 31
	v_cndmask_b32_e32 v2, v2, v3, vcc
	v_rsq_f32_e32 v2, v2
	v_lshlrev_b32_e32 v4, 2, v72
	v_mov_b32_e32 v5, v71
	v_mul_f32_e32 v3, 0x45800000, v2
	v_cndmask_b32_e32 v6, v2, v3, vcc
	v_lshl_add_u64 v[2:3], s[30:31], 0, v[76:77]
	v_or_b32_e32 v2, s14, v2
	s_and_b32 s14, s22, 0x1f80
	v_lshlrev_b64 v[2:3], 15, v[2:3]
	v_lshl_add_u64 v[2:3], s[12:13], 0, v[2:3]
	s_lshl_b32 s14, s14, 2
	v_lshl_add_u64 v[2:3], v[2:3], 0, s[14:15]
	v_lshl_add_u64 v[2:3], v[2:3], 0, v[4:5]
	global_store_dword v[2:3], v6, off
	s_branch .LBB0_399
